# baseline (speedup 1.0000x reference)
.LBB1_12:
	s_mov_b32 s0, s44
	s_add_i32 s44, s44, 1
	s_cmp_ge_u32 s44, s42
	s_cselect_b64 s[22:23], -1, 0
	s_cmp_lt_u32 s44, s42
	s_cselect_b32 s2, s44, s0
	s_waitcnt vmcnt(0)
	s_lshl_b32 s0, s2, 4
	s_mov_b32 s1, s17
	s_mov_b32 m0, s43
	ds_read_b128 v[76:79], v119 offset:32768
	ds_read_b128 v[80:83], v119 offset:36864
	ds_read_b128 v[84:87], v120 offset:32768
	ds_read_b128 v[88:91], v120 offset:36864
	ds_read_b128 v[92:95], v121
	ds_read_b128 v[96:99], v121 offset:4096
	ds_read_b128 v[128:131], v122
	ds_read_b128 v[132:135], v122 offset:4096
	ds_read_b128 v[72:75], v123
	s_waitcnt lgkmcnt(0)
	s_cmp_ge_u32 s44, s42
	s_cbranch_scc1 .Lmain_noids
	v_lshl_add_u64 v[70:71], s[0:1], 2, v[2:3]
	global_load_lds_dword v[70:71], off
.Lmain_noids:
	ds_read_b128 v[156:159], v115
	ds_read_b128 v[160:163], v115 offset:1024
	ds_read_b128 v[164:167], v115 offset:2048
	v_cvt_pk_bf16_f32 v136, v76, v77
	v_cvt_pk_bf16_f32 v137, v78, v79
	v_cvt_pk_bf16_f32 v138, v84, v85
	v_cvt_pk_bf16_f32 v139, v86, v87
	v_cvt_pk_bf16_f32 v140, v92, v93
	v_cvt_pk_bf16_f32 v141, v94, v95
	v_cvt_pk_bf16_f32 v142, v128, v129
	v_cvt_pk_bf16_f32 v143, v130, v131
	v_cvt_pk_bf16_f32 v144, v80, v81
	v_cvt_pk_bf16_f32 v145, v82, v83
	v_cvt_pk_bf16_f32 v146, v88, v89
	v_cvt_pk_bf16_f32 v147, v90, v91
	v_cvt_pk_bf16_f32 v128, v96, v97
	v_cvt_pk_bf16_f32 v129, v98, v99
	v_cvt_pk_bf16_f32 v130, v132, v133
	v_cvt_pk_bf16_f32 v131, v134, v135
	s_lshl_b32 s0, s2, 13
	s_cmp_lt_u32 s44, s42
	s_cselect_b32 s0, s0, 0x1e848000
	s_mov_b32 s61, s0
	s_add_i32 s63, s44, 1
	s_cmp_eq_u32 s63, s42
	s_cselect_b32 s63, 1, 0
	s_cmp_ge_u32 s44, s42
	s_cselect_b32 s63, 2, s63
	ds_read_b128 v[132:135], v115 offset:3072
	s_waitcnt lgkmcnt(3)
	v_mfma_f32_16x16x32_bf16 v[148:151], v[136:139], v[156:159], v[36:39]
	ds_read_b128 v[156:159], v115 offset:4096
	s_waitcnt lgkmcnt(3)
	v_mfma_f32_16x16x32_bf16 v[152:155], v[136:139], v[160:163], v[40:43]
	ds_read_b128 v[160:163], v115 offset:5120
	s_waitcnt lgkmcnt(3)
	v_mfma_f32_16x16x32_bf16 v[96:99], v[136:139], v[164:167], v[44:47]
	ds_read_b128 v[164:167], v115 offset:6144
	s_waitcnt lgkmcnt(3)
	v_mfma_f32_16x16x32_bf16 v[92:95], v[136:139], v[132:135], v[48:51]
	ds_read_b128 v[132:135], v115 offset:7168
	s_waitcnt lgkmcnt(3)
	v_mfma_f32_16x16x32_bf16 v[88:91], v[136:139], v[156:159], v[52:55]
	ds_read_b128 v[156:159], v115 offset:8192
	s_waitcnt lgkmcnt(3)
	v_mfma_f32_16x16x32_bf16 v[84:87], v[136:139], v[160:163], v[56:59]
	ds_read_b128 v[160:163], v115 offset:9216
	s_waitcnt lgkmcnt(3)
	v_mfma_f32_16x16x32_bf16 v[80:83], v[136:139], v[164:167], v[60:63]
	ds_read_b128 v[164:167], v115 offset:10240
	s_waitcnt lgkmcnt(3)
	v_mfma_f32_16x16x32_bf16 v[76:79], v[136:139], v[132:135], v[64:67]
	ds_read_b128 v[132:135], v115 offset:11264
	s_waitcnt lgkmcnt(3)
	v_mfma_f32_16x16x32_bf16 v[148:151], v[140:143], v[156:159], v[148:151]
	ds_read_b128 v[156:159], v115 offset:12288
	s_waitcnt lgkmcnt(3)
	v_mfma_f32_16x16x32_bf16 v[152:155], v[140:143], v[160:163], v[152:155]
	ds_read_b128 v[160:163], v115 offset:13312
	s_waitcnt lgkmcnt(3)
	v_mfma_f32_16x16x32_bf16 v[96:99], v[140:143], v[164:167], v[96:99]
	ds_read_b128 v[164:167], v115 offset:14336
	s_waitcnt lgkmcnt(3)
	v_mfma_f32_16x16x32_bf16 v[92:95], v[140:143], v[132:135], v[92:95]
	ds_read_b128 v[132:135], v115 offset:15360
	s_waitcnt lgkmcnt(3)
	v_mfma_f32_16x16x32_bf16 v[88:91], v[140:143], v[156:159], v[88:91]
	ds_read_b128 v[156:159], v115 offset:16384
	s_waitcnt lgkmcnt(3)
	v_mfma_f32_16x16x32_bf16 v[84:87], v[140:143], v[160:163], v[84:87]
	ds_read_b128 v[160:163], v115 offset:17408
	s_waitcnt lgkmcnt(3)
	v_mfma_f32_16x16x32_bf16 v[80:83], v[140:143], v[164:167], v[80:83]
	ds_read_b128 v[164:167], v115 offset:18432
	s_waitcnt lgkmcnt(3)
	v_mfma_f32_16x16x32_bf16 v[76:79], v[140:143], v[132:135], v[76:79]
	ds_read_b128 v[132:135], v115 offset:19456
	s_waitcnt lgkmcnt(3)
	s_cmp_eq_u32 s63, 2
	s_cbranch_scc1 .Lmain_noburst
	s_mov_b32 m0, s47
	s_nop 0
	buffer_load_dwordx4 v113, s[12:15], s61 offen nt lds
	s_cmp_eq_u32 s63, 0
	s_cbranch_scc1 .Lmain_noburst
	s_or_b32 s62, s61, 0x800
	s_mov_b32 m0, s48
	s_nop 0
	buffer_load_dwordx4 v113, s[12:15], s62 offen nt lds
	s_or_b32 s62, s61, 0x1000
	s_mov_b32 m0, s49
	s_nop 0
	buffer_load_dwordx4 v113, s[12:15], s62 offen nt lds
	s_or_b32 s62, s61, 0x1800
	s_mov_b32 m0, s50
	s_nop 0
	buffer_load_dwordx4 v113, s[12:15], s62 offen nt lds
	s_or_b32 s62, s61, 0x100
	s_mov_b32 m0, s51
	s_nop 0
	buffer_load_dwordx4 v113, s[12:15], s62 offen nt lds
	s_or_b32 s62, s61, 0x900
	s_mov_b32 m0, s52
	s_nop 0
	buffer_load_dwordx4 v113, s[12:15], s62 offen nt lds
	s_or_b32 s62, s61, 0x1100
	s_mov_b32 m0, s53
	s_nop 0
	buffer_load_dwordx4 v113, s[12:15], s62 offen nt lds
	s_or_b32 s62, s61, 0x1900
	s_mov_b32 m0, s54
	s_nop 0
	buffer_load_dwordx4 v113, s[12:15], s62 offen nt lds
